# prologue expert conversion row loads without the non-temporal hint
# speedup vs baseline: 1.0042x; 1.0012x over previous
.LBB0_41:
	s_add_i32 s23, s22, 0xffffc000
	s_cmpk_gt_i32 s22, 0x3fff
	v_readlane_b32 s48, v253, 58
	s_cselect_b64 s[44:45], -1, 0
	v_readlane_b32 s49, v253, 59
	v_readlane_b32 s50, v253, 60
	v_readlane_b32 s51, v253, 61
	v_readlane_b32 s60, v254, 6
	v_readlane_b32 s61, v254, 7
	s_and_b64 s[24:25], s[44:45], exec
	v_readlane_b32 s62, v254, 8
	v_readlane_b32 s63, v254, 9
	s_mov_b64 s[48:49], s[60:61]
	s_cselect_b32 s24, s23, s22
	s_mov_b64 s[50:51], s[62:63]
	s_mov_b32 s23, 0x12b00000
	s_cselect_b32 s26, s51, s49
	s_cselect_b32 s27, s50, s48
	s_cselect_b32 s23, s23, 0xab00000
	s_add_i32 s86, s24, s16
	s_ashr_i32 s87, s86, 31
	s_lshl_b64 s[24:25], s[86:87], 13
	s_add_u32 s24, s27, s24
	s_addc_u32 s25, s26, s25
	v_lshl_add_u64 v[62:63], v[22:23], 2, s[24:25]
	s_movk_i32 s24, 0x1000
	global_load_dwordx4 v[2:5], v[62:63], off
	global_load_dwordx4 v[6:9], v[62:63], off offset:1024
	global_load_dwordx4 v[10:13], v[62:63], off offset:2048
	global_load_dwordx4 v[14:17], v[62:63], off offset:3072
	v_add_co_u32_e32 v86, vcc, s24, v62
	s_add_u32 s23, s10, s23
	s_nop 0
	v_addc_co_u32_e32 v87, vcc, 0, v63, vcc
	global_load_dwordx4 v[62:65], v[86:87], off
	global_load_dwordx4 v[66:69], v[86:87], off offset:1024
	global_load_dwordx4 v[82:85], v[86:87], off offset:2048
	s_nop 0
	global_load_dwordx4 v[86:89], v[86:87], off offset:3072
	v_readlane_b32 s52, v253, 62
	v_readlane_b32 s53, v253, 63
	v_readlane_b32 s54, v254, 0
	v_readlane_b32 s55, v254, 1
	v_readlane_b32 s56, v254, 2
	v_readlane_b32 s57, v254, 3
	v_readlane_b32 s58, v254, 4
	v_readlane_b32 s59, v254, 5
	s_waitcnt vmcnt(7)
	v_max_f32_e64 v55, |v5|, |v5|
	v_max_f32_e64 v57, |v4|, |v4|
	s_waitcnt vmcnt(6)
	v_max_f32_e64 v61, |v9|, |v9|
	v_max_f32_e64 v70, |v8|, |v8|
	s_waitcnt vmcnt(5)
	v_max_f32_e64 v72, |v13|, |v13|
	v_max_f32_e64 v74, |v12|, |v12|
	s_waitcnt vmcnt(4)
	v_max_f32_e64 v81, |v17|, |v17|
	v_max_f32_e64 v90, |v16|, |v16|
	v_max_f32_e32 v55, v57, v55
	v_max_f32_e32 v57, v70, v61
	v_max_f32_e32 v61, v74, v72
	v_max_f32_e32 v70, v90, v81
	s_waitcnt vmcnt(3)
	v_max_f32_e64 v72, |v65|, |v65|
	v_max_f32_e64 v74, |v64|, |v64|
	s_waitcnt vmcnt(2)
	v_max_f32_e64 v81, |v69|, |v69|
	v_max_f32_e64 v90, |v68|, |v68|
	v_max3_f32 v55, |v2|, |v3|, v55
	v_max3_f32 v57, |v6|, |v7|, v57
	s_waitcnt vmcnt(1)
	v_max_f32_e64 v91, |v85|, |v85|
	v_max_f32_e64 v92, |v84|, |v84|
	s_waitcnt vmcnt(0)
	v_max_f32_e64 v93, |v89|, |v89|
	v_max_f32_e64 v94, |v88|, |v88|
	v_max3_f32 v61, |v10|, |v11|, v61
	v_max3_f32 v70, |v14|, |v15|, v70
	v_max_f32_e32 v72, v74, v72
	v_max_f32_e32 v74, v90, v81
	v_max3_f32 v55, v55, 0, v57
	v_max_f32_e32 v81, v92, v91
	v_max_f32_e32 v90, v94, v93
	v_max3_f32 v57, |v62|, |v63|, v72
	v_max3_f32 v72, |v66|, |v67|, v74
	v_max3_f32 v55, v55, v61, v70
	v_max3_f32 v74, |v82|, |v83|, v81
	v_max3_f32 v81, |v86|, |v87|, v90
	v_max3_f32 v55, v55, v57, v72
	v_max3_f32 v55, v55, v74, v81
	s_nop 1
	v_mov_b32_dpp v57, v55 quad_perm:[1,0,3,2] row_mask:0xf bank_mask:0xf bound_ctrl:1
	v_max_f32_e32 v57, v57, v57
	v_max_f32_e32 v55, v55, v57
	s_nop 1
	v_mov_b32_dpp v57, v55 quad_perm:[2,3,0,1] row_mask:0xf bank_mask:0xf bound_ctrl:1
	v_max_f32_e32 v57, v57, v57
	v_max_f32_e32 v55, v55, v57
	s_nop 1
	v_mov_b32_dpp v57, v55 row_half_mirror row_mask:0xf bank_mask:0xf bound_ctrl:1
	v_max_f32_e32 v57, v57, v57
	v_max_f32_e32 v55, v55, v57
	s_nop 1
	v_mov_b32_dpp v57, v55 row_mirror row_mask:0xf bank_mask:0xf bound_ctrl:1
	v_max_f32_e32 v57, v57, v57
	v_max_f32_e32 v55, v55, v57
	s_nop 0
	v_readlane_b32 s26, v55, 32
	v_readlane_b32 s27, v55, 48
	v_readlane_b32 s24, v55, 0
	v_readlane_b32 s25, v55, 16
	v_max_f32_e64 v55, s27, s27
	v_max_f32_e64 v57, s26, s26
	v_mov_b32_e32 v61, s25
	v_max_f32_e32 v55, v57, v55
	v_max3_f32 v55, s24, v61, v55
	v_mul_f32_e32 v57, 0x3e088889, v55
	v_cmp_lt_f32_e32 vcc, 0, v55
	s_mul_hi_i32 s26, s86, 0x600
	s_nop 0
	v_cndmask_b32_e32 v55, 1.0, v57, vcc
	v_div_scale_f32 v57, s[24:25], v55, v55, 1.0
	v_rcp_f32_e32 v61, v57
	v_div_scale_f32 v70, vcc, 1.0, v55, 1.0
	s_addc_u32 s25, s11, 0
	v_fma_f32 v72, -v57, v61, 1.0
	v_fmac_f32_e32 v61, v72, v61
	v_mul_f32_e32 v72, v70, v61
	v_fma_f32 v74, -v57, v72, v70
	v_fmac_f32_e32 v72, v74, v61
	v_fma_f32 v57, -v57, v72, v70
	v_div_fmas_f32 v57, v57, v61, v72
	v_div_fixup_f32 v70, v57, v55, 1.0
	s_mul_i32 s24, s86, 0x600
	v_pk_mul_f32 v[2:3], v[2:3], v[70:71] op_sel_hi:[1,0]
	v_pk_mul_f32 v[4:5], v[4:5], v[70:71] op_sel_hi:[1,0]
	v_pk_mul_f32 v[6:7], v[6:7], v[70:71] op_sel_hi:[1,0]
	v_pk_mul_f32 v[8:9], v[8:9], v[70:71] op_sel_hi:[1,0]
	v_pk_mul_f32 v[10:11], v[10:11], v[70:71] op_sel_hi:[1,0]
	v_pk_mul_f32 v[12:13], v[12:13], v[70:71] op_sel_hi:[1,0]
	v_pk_mul_f32 v[14:15], v[14:15], v[70:71] op_sel_hi:[1,0]
	v_pk_mul_f32 v[16:17], v[16:17], v[70:71] op_sel_hi:[1,0]
	v_pk_mul_f32 v[62:63], v[62:63], v[70:71] op_sel_hi:[1,0]
	v_pk_mul_f32 v[64:65], v[64:65], v[70:71] op_sel_hi:[1,0]
	v_pk_mul_f32 v[66:67], v[66:67], v[70:71] op_sel_hi:[1,0]
	v_pk_mul_f32 v[68:69], v[68:69], v[70:71] op_sel_hi:[1,0]
	v_pk_mul_f32 v[82:83], v[82:83], v[70:71] op_sel_hi:[1,0]
	v_pk_mul_f32 v[84:85], v[84:85], v[70:71] op_sel_hi:[1,0]
	v_pk_mul_f32 v[86:87], v[86:87], v[70:71] op_sel_hi:[1,0]
	v_pk_mul_f32 v[88:89], v[88:89], v[70:71] op_sel_hi:[1,0]
	s_add_u32 s24, s23, s24
	v_cvt_pk_bf16_f32 v2, v2, v3
	v_cvt_pk_bf16_f32 v3, v4, v5
	v_cvt_pk_bf16_f32 v4, v6, v7
	v_cvt_pk_bf16_f32 v5, v8, v9
	v_cvt_pk_bf16_f32 v6, v10, v11
	v_cvt_pk_bf16_f32 v7, v12, v13
	v_cvt_pk_bf16_f32 v8, v14, v15
	v_cvt_pk_bf16_f32 v9, v16, v17
	v_cvt_pk_bf16_f32 v10, v62, v63
	v_cvt_pk_bf16_f32 v11, v64, v65
	v_cvt_pk_bf16_f32 v12, v66, v67
	v_cvt_pk_bf16_f32 v13, v68, v69
	v_cvt_pk_bf16_f32 v14, v82, v83
	v_cvt_pk_bf16_f32 v15, v84, v85
	v_cvt_pk_bf16_f32 v16, v86, v87
	v_cvt_pk_bf16_f32 v17, v88, v89
	s_addc_u32 s25, s25, s26
	v_cvt_scalef32_pk32_fp6_bf16 v[62:67], v[2:17], 1.0
	v_lshl_add_u64 v[2:3], s[24:25], 0, v[44:45]
	global_store_dwordx4 v[2:3], v[62:65], off
	v_lshl_add_u64 v[2:3], s[24:25], 0, v[30:31]
	global_store_dwordx2 v[2:3], v[66:67], off offset:1024
	s_and_saveexec_b64 s[68:69], s[2:3]
	s_cbranch_execz .LBB0_40
	s_and_b64 s[24:25], s[44:45], exec
	s_mov_b32 s23, 0x1ac00000
	s_cselect_b32 s23, s23, 0x1ab00000
	s_add_u32 s23, s10, s23
	s_addc_u32 s26, s11, 0
	s_lshl_b64 s[24:25], s[86:87], 2
	s_add_u32 s24, s23, s24
	s_addc_u32 s25, s26, s25
	global_store_dword v18, v55, s[24:25]
	s_branch .LBB0_40
